# k_agg1 epilogue: W2 LDS reads double-buffered one feature ahead
# baseline (speedup 1.0000x reference)
.LBB3_12:
	ds_read_b128 v[58:61], v22 offset:2048
	ds_read_b128 v[0:3], v22 offset:2064
	ds_read_b128 v[34:37], v23
	ds_read_b128 v[38:41], v23 offset:16
	ds_read_b128 v[50:53], v23 offset:256
	ds_read_b128 v[54:57], v23 offset:272
	s_waitcnt vmcnt(0) lgkmcnt(4)
	v_fma_f32 v32, v29, v18, v58
	v_max_f32_e32 v32, 0, v32
	v_mul_f32_e32 v32, v29, v32
	s_waitcnt lgkmcnt(2)
	v_pk_fma_f32 v[42:43], v[32:33], v[34:35], 0 op_sel_hi:[0,1,0]
	v_pk_fma_f32 v[44:45], v[32:33], v[36:37], 0 op_sel_hi:[0,1,0]
	v_pk_fma_f32 v[46:47], v[32:33], v[38:39], 0 op_sel_hi:[0,1,0]
	v_pk_fma_f32 v[48:49], v[32:33], v[40:41], 0 op_sel_hi:[0,1,0]
	ds_read_b128 v[34:37], v23 offset:512
	ds_read_b128 v[38:41], v23 offset:528
	v_fma_f32 v32, v29, v19, v59
	v_max_f32_e32 v32, 0, v32
	v_mul_f32_e32 v32, v29, v32
	s_waitcnt lgkmcnt(2)
	v_pk_fma_f32 v[42:43], v[32:33], v[50:51], v[42:43] op_sel_hi:[0,1,1]
	v_pk_fma_f32 v[44:45], v[32:33], v[52:53], v[44:45] op_sel_hi:[0,1,1]
	v_pk_fma_f32 v[46:47], v[32:33], v[54:55], v[46:47] op_sel_hi:[0,1,1]
	v_pk_fma_f32 v[48:49], v[32:33], v[56:57], v[48:49] op_sel_hi:[0,1,1]
	ds_read_b128 v[50:53], v23 offset:768
	ds_read_b128 v[54:57], v23 offset:784
	v_fma_f32 v32, v29, v16, v60
	v_max_f32_e32 v32, 0, v32
	v_mul_f32_e32 v32, v29, v32
	s_waitcnt lgkmcnt(2)
	v_pk_fma_f32 v[42:43], v[32:33], v[34:35], v[42:43] op_sel_hi:[0,1,1]
	v_pk_fma_f32 v[44:45], v[32:33], v[36:37], v[44:45] op_sel_hi:[0,1,1]
	v_pk_fma_f32 v[46:47], v[32:33], v[38:39], v[46:47] op_sel_hi:[0,1,1]
	v_pk_fma_f32 v[48:49], v[32:33], v[40:41], v[48:49] op_sel_hi:[0,1,1]
	ds_read_b128 v[34:37], v23 offset:1024
	ds_read_b128 v[38:41], v23 offset:1040
	v_fma_f32 v32, v29, v17, v61
	v_max_f32_e32 v32, 0, v32
	v_mul_f32_e32 v32, v29, v32
	s_waitcnt lgkmcnt(2)
	v_pk_fma_f32 v[42:43], v[32:33], v[50:51], v[42:43] op_sel_hi:[0,1,1]
	v_pk_fma_f32 v[44:45], v[32:33], v[52:53], v[44:45] op_sel_hi:[0,1,1]
	v_pk_fma_f32 v[46:47], v[32:33], v[54:55], v[46:47] op_sel_hi:[0,1,1]
	v_pk_fma_f32 v[48:49], v[32:33], v[56:57], v[48:49] op_sel_hi:[0,1,1]
	ds_read_b128 v[50:53], v23 offset:1280
	ds_read_b128 v[54:57], v23 offset:1296
	v_fma_f32 v32, v29, v14, v0
	v_max_f32_e32 v32, 0, v32
	v_mul_f32_e32 v32, v29, v32
	s_waitcnt lgkmcnt(2)
	v_pk_fma_f32 v[42:43], v[32:33], v[34:35], v[42:43] op_sel_hi:[0,1,1]
	v_pk_fma_f32 v[44:45], v[32:33], v[36:37], v[44:45] op_sel_hi:[0,1,1]
	v_pk_fma_f32 v[46:47], v[32:33], v[38:39], v[46:47] op_sel_hi:[0,1,1]
	v_pk_fma_f32 v[48:49], v[32:33], v[40:41], v[48:49] op_sel_hi:[0,1,1]
	ds_read_b128 v[34:37], v23 offset:1536
	ds_read_b128 v[38:41], v23 offset:1552
	v_fma_f32 v32, v29, v15, v1
	v_max_f32_e32 v32, 0, v32
	v_mul_f32_e32 v32, v29, v32
	s_waitcnt lgkmcnt(2)
	v_pk_fma_f32 v[42:43], v[32:33], v[50:51], v[42:43] op_sel_hi:[0,1,1]
	v_pk_fma_f32 v[44:45], v[32:33], v[52:53], v[44:45] op_sel_hi:[0,1,1]
	v_pk_fma_f32 v[46:47], v[32:33], v[54:55], v[46:47] op_sel_hi:[0,1,1]
	v_pk_fma_f32 v[48:49], v[32:33], v[56:57], v[48:49] op_sel_hi:[0,1,1]
	ds_read_b128 v[50:53], v23 offset:1792
	ds_read_b128 v[54:57], v23 offset:1808
	v_fma_f32 v32, v29, v12, v2
	v_max_f32_e32 v32, 0, v32
	v_mul_f32_e32 v32, v29, v32
	s_waitcnt lgkmcnt(2)
	v_pk_fma_f32 v[42:43], v[32:33], v[34:35], v[42:43] op_sel_hi:[0,1,1]
	v_pk_fma_f32 v[44:45], v[32:33], v[36:37], v[44:45] op_sel_hi:[0,1,1]
	v_pk_fma_f32 v[46:47], v[32:33], v[38:39], v[46:47] op_sel_hi:[0,1,1]
	v_pk_fma_f32 v[48:49], v[32:33], v[40:41], v[48:49] op_sel_hi:[0,1,1]
	v_fma_f32 v32, v29, v13, v3
	v_max_f32_e32 v32, 0, v32
	v_mul_f32_e32 v32, v29, v32
	s_waitcnt lgkmcnt(0)
	v_pk_fma_f32 v[42:43], v[32:33], v[50:51], v[42:43] op_sel_hi:[0,1,1]
	v_pk_fma_f32 v[44:45], v[32:33], v[52:53], v[44:45] op_sel_hi:[0,1,1]
	v_pk_fma_f32 v[46:47], v[32:33], v[54:55], v[46:47] op_sel_hi:[0,1,1]
	v_pk_fma_f32 v[48:49], v[32:33], v[56:57], v[48:49] op_sel_hi:[0,1,1]
	v_add_f32_dpp v0, v42, v42 quad_perm:[1,0,3,2] row_mask:0xf bank_mask:0xf bound_ctrl:1
	v_add_f32_dpp v2, v43, v43 quad_perm:[1,0,3,2] row_mask:0xf bank_mask:0xf bound_ctrl:1
	v_add_f32_dpp v12, v44, v44 quad_perm:[1,0,3,2] row_mask:0xf bank_mask:0xf bound_ctrl:1
	v_add_f32_dpp v14, v45, v45 quad_perm:[1,0,3,2] row_mask:0xf bank_mask:0xf bound_ctrl:1
	v_add_f32_dpp v16, v46, v46 quad_perm:[1,0,3,2] row_mask:0xf bank_mask:0xf bound_ctrl:1
	v_add_f32_dpp v18, v47, v47 quad_perm:[1,0,3,2] row_mask:0xf bank_mask:0xf bound_ctrl:1
	v_add_f32_dpp v29, v48, v48 quad_perm:[1,0,3,2] row_mask:0xf bank_mask:0xf bound_ctrl:1
	v_add_f32_dpp v0, v0, v0 quad_perm:[2,3,0,1] row_mask:0xf bank_mask:0xf bound_ctrl:1
	v_add_f32_dpp v2, v2, v2 quad_perm:[2,3,0,1] row_mask:0xf bank_mask:0xf bound_ctrl:1
	v_add_f32_dpp v12, v12, v12 quad_perm:[2,3,0,1] row_mask:0xf bank_mask:0xf bound_ctrl:1
	v_add_f32_dpp v14, v14, v14 quad_perm:[2,3,0,1] row_mask:0xf bank_mask:0xf bound_ctrl:1
	v_add_f32_dpp v16, v16, v16 quad_perm:[2,3,0,1] row_mask:0xf bank_mask:0xf bound_ctrl:1
	v_add_f32_dpp v18, v18, v18 quad_perm:[2,3,0,1] row_mask:0xf bank_mask:0xf bound_ctrl:1
	v_add_f32_dpp v29, v29, v29 quad_perm:[2,3,0,1] row_mask:0xf bank_mask:0xf bound_ctrl:1
	v_mov_b32_dpp v1, v0 row_half_mirror row_mask:0xf bank_mask:0xf bound_ctrl:1
	v_mov_b32_dpp v3, v2 row_half_mirror row_mask:0xf bank_mask:0xf bound_ctrl:1
	v_mov_b32_dpp v13, v12 row_half_mirror row_mask:0xf bank_mask:0xf bound_ctrl:1
	v_mov_b32_dpp v15, v14 row_half_mirror row_mask:0xf bank_mask:0xf bound_ctrl:1
	v_mov_b32_dpp v17, v16 row_half_mirror row_mask:0xf bank_mask:0xf bound_ctrl:1
	v_mov_b32_dpp v19, v18 row_half_mirror row_mask:0xf bank_mask:0xf bound_ctrl:1
	v_mov_b32_dpp v30, v29 row_half_mirror row_mask:0xf bank_mask:0xf bound_ctrl:1
	s_and_saveexec_b64 s[18:19], s[4:5]
	s_cbranch_execz .LBB3_1
	v_add_f32_e32 v2, v2, v3
	v_add_f32_e32 v0, v0, v1
	v_add_f32_e32 v12, v12, v13
	v_cndmask_b32_e64 v0, v0, v2, s[6:7]
	v_add_f32_e32 v14, v14, v15
	v_cndmask_b32_e64 v0, v0, v12, s[8:9]
	v_add_f32_e32 v16, v16, v17
	v_cndmask_b32_e64 v0, v0, v14, s[10:11]
	v_add_f32_e32 v18, v18, v19
	v_cndmask_b32_e64 v0, v0, v16, s[12:13]
	v_add_f32_e32 v29, v29, v30
	v_cndmask_b32_e64 v0, v0, v18, s[14:15]
	v_cndmask_b32_e64 v2, v0, v29, s[16:17]
	v_lshlrev_b64 v[0:1], 5, v[4:5]
	v_lshl_add_u64 v[0:1], v[10:11], 0, v[0:1]
	global_atomic_add_f32 v[0:1], v2, off
	s_branch .LBB3_1
